# speedup vs baseline: 1.1016x; 1.0042x over previous
.Lret2:
	s_waitcnt vmcnt(9)
	v_cvt_pk_f16_f32 v79, v8, v9
	v_cvt_pk_f16_f32 v78, v6, v7
	ds_write_b64 v141, v[78:79] offset:19456
	s_waitcnt vmcnt(8)
	v_cvt_pk_f16_f32 v79, v12, v13
	v_cvt_pk_f16_f32 v78, v10, v11
	ds_write_b64 v143, v[78:79] offset:19456
	s_waitcnt vmcnt(7)
	v_cvt_pk_f16_f32 v79, v20, v21
	v_cvt_pk_f16_f32 v78, v18, v19
	ds_write_b64 v144, v[78:79] offset:19456
	s_waitcnt vmcnt(6)
	v_cvt_pk_f16_f32 v79, v24, v25
	v_cvt_pk_f16_f32 v78, v22, v23
	ds_write_b64 v145, v[78:79] offset:19456
	s_waitcnt vmcnt(5)
	v_cvt_pk_f16_f32 v79, v28, v29
	v_cvt_pk_f16_f32 v78, v26, v27
	ds_write_b64 v146, v[78:79] offset:19456
	s_waitcnt vmcnt(4)
	v_cvt_pk_f16_f32 v79, v32, v33
	v_cvt_pk_f16_f32 v78, v30, v31
	ds_write_b64 v147, v[78:79] offset:19456
	s_waitcnt vmcnt(3)
	v_cvt_pk_f16_f32 v79, v40, v41
	v_cvt_pk_f16_f32 v78, v38, v39
	ds_write_b64 v141, v[78:79] offset:22568
	s_waitcnt vmcnt(2)
	v_cvt_pk_f16_f32 v79, v44, v45
	v_cvt_pk_f16_f32 v78, v42, v43
	ds_write_b64 v148, v[78:79] offset:19456
	s_waitcnt vmcnt(1)
	v_cvt_pk_f16_f32 v79, v52, v53
	v_cvt_pk_f16_f32 v78, v50, v51
	ds_write_b64 v149, v[78:79] offset:19456
	s_mov_b32 s3, 3
	v_mov_b32_e32 v86, 0
	v_mov_b32_e32 v78, 0
	v_mov_b32_e32 v79, 0
	v_mov_b32_e32 v80, 0
	v_mov_b32_e32 v81, 0
	v_mov_b32_e32 v82, 0
	v_mov_b32_e32 v83, 0
	v_mov_b32_e32 v84, 0
	v_mov_b32_e32 v85, 0
	ds_read_b128 v[194:197], v142
	ds_read_b128 v[198:201], v136
	ds_read_b128 v[202:205], v136 offset:9728
	ds_read_b128 v[206:209], v142 offset:64
	ds_read_b128 v[210:213], v136 offset:64
	ds_read_b128 v[214:217], v136 offset:9792
	ds_read_b128 v[218:221], v142 offset:128
	ds_read_b128 v[222:225], v136 offset:128
	ds_read_b128 v[226:229], v136 offset:9856
	ds_read_b128 v[230:233], v142 offset:192
	ds_read_b128 v[234:237], v136 offset:192
	ds_read_b128 v[238:241], v136 offset:9920
	s_waitcnt lgkmcnt(9)
	v_mfma_f32_16x16x32_f16 v[78:81], v[194:197], v[198:201], v[78:81]
	v_dot2c_f32_f16_e32 v86, v194, v194
	v_dot2c_f32_f16_e32 v86, v195, v195
	v_mfma_f32_16x16x32_f16 v[82:85], v[194:197], v[202:205], v[82:85]
	v_dot2c_f32_f16_e32 v86, v196, v196
	v_dot2c_f32_f16_e32 v86, v197, v197
	ds_read_b128 v[194:197], v142 offset:256
	ds_read_b128 v[198:201], v136 offset:256
	ds_read_b128 v[202:205], v136 offset:9984
	s_waitcnt lgkmcnt(9)
	v_mfma_f32_16x16x32_f16 v[78:81], v[206:209], v[210:213], v[78:81]
	v_dot2c_f32_f16_e32 v86, v206, v206
	v_dot2c_f32_f16_e32 v86, v207, v207
	v_mfma_f32_16x16x32_f16 v[82:85], v[206:209], v[214:217], v[82:85]
	v_dot2c_f32_f16_e32 v86, v208, v208
	v_dot2c_f32_f16_e32 v86, v209, v209
	ds_read_b128 v[206:209], v142 offset:320
	ds_read_b128 v[210:213], v136 offset:320
	ds_read_b128 v[214:217], v136 offset:10048
	s_waitcnt lgkmcnt(9)
	v_mfma_f32_16x16x32_f16 v[78:81], v[218:221], v[222:225], v[78:81]
	v_dot2c_f32_f16_e32 v86, v218, v218
	v_dot2c_f32_f16_e32 v86, v219, v219
	v_mfma_f32_16x16x32_f16 v[82:85], v[218:221], v[226:229], v[82:85]
	v_dot2c_f32_f16_e32 v86, v220, v220
	v_dot2c_f32_f16_e32 v86, v221, v221
	s_waitcnt lgkmcnt(6)
	v_mfma_f32_16x16x32_f16 v[78:81], v[230:233], v[234:237], v[78:81]
	v_dot2c_f32_f16_e32 v86, v230, v230
	v_dot2c_f32_f16_e32 v86, v231, v231
	v_mfma_f32_16x16x32_f16 v[82:85], v[230:233], v[238:241], v[82:85]
	v_dot2c_f32_f16_e32 v86, v232, v232
	v_dot2c_f32_f16_e32 v86, v233, v233
	s_waitcnt lgkmcnt(3)
	v_mfma_f32_16x16x32_f16 v[78:81], v[194:197], v[198:201], v[78:81]
	v_dot2c_f32_f16_e32 v86, v194, v194
	v_dot2c_f32_f16_e32 v86, v195, v195
	v_mfma_f32_16x16x32_f16 v[82:85], v[194:197], v[202:205], v[82:85]
	v_dot2c_f32_f16_e32 v86, v196, v196
	v_dot2c_f32_f16_e32 v86, v197, v197
	s_waitcnt lgkmcnt(0)
	v_mfma_f32_16x16x32_f16 v[78:81], v[206:209], v[210:213], v[78:81]
	v_dot2c_f32_f16_e32 v86, v206, v206
	v_dot2c_f32_f16_e32 v86, v207, v207
	v_mfma_f32_16x16x32_f16 v[82:85], v[206:209], v[214:217], v[82:85]
	v_dot2c_f32_f16_e32 v86, v208, v208
	v_dot2c_f32_f16_e32 v86, v209, v209
	ds_read_b128 v[222:225], v136 offset:384
	ds_read_b128 v[226:229], v136 offset:10112
	ds_read_b128 v[234:237], v136 offset:448
	ds_read_b128 v[238:241], v136 offset:10176
	ds_read_b128 v[198:201], v136 offset:512
	ds_read_b128 v[202:205], v136 offset:10240
	ds_read2st64_b64 v[88:91], v160 offset0:1 offset1:20
	s_waitcnt vmcnt(0)
	v_cvt_pk_f16_f32 v163, v188, v189
	v_cvt_pk_f16_f32 v162, v186, v187
	s_and_saveexec_b64 s[12:13], s[8:9]
	ds_write_b64 v150, v[162:163] offset:19456
	s_or_b64 exec, exec, s[12:13]
	ds_read_b128 v[218:221], v142 offset:384
	ds_read_b128 v[230:233], v142 offset:448
	ds_read_b128 v[194:197], v142 offset:512
	ds_read_b64 v[92:93], v159 offset:20032
	s_waitcnt lgkmcnt(3)
	v_mfma_f32_16x16x32_f16 v[78:81], v[218:221], v[222:225], v[78:81]
	v_dot2c_f32_f16_e32 v86, v218, v218
	v_dot2c_f32_f16_e32 v86, v219, v219
	v_mfma_f32_16x16x32_f16 v[82:85], v[218:221], v[226:229], v[82:85]
	v_dot2c_f32_f16_e32 v86, v220, v220
	v_dot2c_f32_f16_e32 v86, v221, v221
	s_waitcnt lgkmcnt(2)
	v_mfma_f32_16x16x32_f16 v[78:81], v[230:233], v[234:237], v[78:81]
	v_dot2c_f32_f16_e32 v86, v230, v230
	v_dot2c_f32_f16_e32 v86, v231, v231
	v_mfma_f32_16x16x32_f16 v[82:85], v[230:233], v[238:241], v[82:85]
	v_dot2c_f32_f16_e32 v86, v232, v232
	v_dot2c_f32_f16_e32 v86, v233, v233
	s_waitcnt lgkmcnt(1)
	v_mfma_f32_16x16x32_f16 v[78:81], v[194:197], v[198:201], v[78:81]
	v_dot2c_f32_f16_e32 v86, v194, v194
	v_dot2c_f32_f16_e32 v86, v195, v195
	v_mfma_f32_16x16x32_f16 v[82:85], v[194:197], v[202:205], v[82:85]
	v_dot2c_f32_f16_e32 v86, v196, v196
	v_dot2c_f32_f16_e32 v86, v197, v197
	s_waitcnt lgkmcnt(0)
	v_mfma_f32_16x16x16_f16 v[78:81], v[92:93], v[88:89], v[78:81]
	v_dot2c_f32_f16_e32 v86, v92, v92
	v_dot2c_f32_f16_e32 v86, v93, v93
	v_mfma_f32_16x16x16_f16 v[82:85], v[92:93], v[90:91], v[82:85]
	s_branch .Lnorm

.Lnorm:
	s_nop 1
	v_mov_b32_e32 v87, v86
	s_nop 1
	v_permlane16_swap_b32_e32 v87, v86
	v_add_f32_e32 v86, v86, v87
	v_mov_b32_e32 v87, v86
	s_nop 1
	v_permlane32_swap_b32_e32 v87, v86
	v_add_f32_e32 v86, v86, v87
	v_mul_f32_e32 v87, 0x4f800000, v86
	v_cmp_gt_f32_e32 vcc, s21, v86
	s_nop 1
	v_cndmask_b32_e32 v86, v86, v87, vcc
	v_sqrt_f32_e32 v87, v86
	s_nop 0
	v_add_u32_e32 v88, -1, v87
	v_fma_f32 v90, -v88, v87, v86
	v_add_u32_e32 v89, 1, v87
	v_cmp_ge_f32_e64 s[12:13], 0, v90
	s_nop 1
	v_cndmask_b32_e64 v88, v87, v88, s[12:13]
	v_fma_f32 v87, -v89, v87, v86
	v_cmp_lt_f32_e64 s[12:13], 0, v87
	s_nop 1
	v_cndmask_b32_e64 v87, v88, v89, s[12:13]
	v_mul_f32_e32 v88, 0x37800000, v87
	v_cndmask_b32_e32 v87, v87, v88, vcc
	v_cmp_class_f32_e32 vcc, v86, v135
	s_nop 1
	v_cndmask_b32_e32 v86, v87, v86, vcc
	v_add_f32_e32 v86, 0x29e12e13, v86
	v_div_scale_f32 v87, s[12:13], v86, v86, 1.0
	v_rcp_f32_e32 v88, v87
	v_lshrrev_b32_e32 v89, s3, v191
	v_and_b32_e32 v89, 1, v89
	s_nop 0
	v_fma_f32 v90, -v87, v88, 1.0
	v_fmac_f32_e32 v88, v90, v88
	v_div_scale_f32 v90, vcc, 1.0, v86, 1.0
	v_mul_f32_e32 v91, v90, v88
	v_fma_f32 v92, -v87, v91, v90
	v_fmac_f32_e32 v91, v92, v88
	v_fma_f32 v87, -v87, v91, v90
	v_div_fmas_f32 v87, v87, v88, v91
	v_div_fixup_f32 v86, v87, v86, 1.0
	v_mul_f32_e32 v86, 0x4166d4ca, v86
	v_cmp_eq_u32_e32 vcc, 1, v89
	s_nop 1
	v_cndmask_b32_e32 v86, 0, v86, vcc
	v_cndmask_b32_e64 v87, v161, 0, vcc
	s_and_saveexec_b64 s[24:25], s[4:5]
	ds_write2_b32 v139, v86, v87 offset1:16
	s_or_b64 exec, exec, s[24:25]
	ds_read_b64 v[88:89], v140
	ds_read_b64 v[90:91], v140 offset:64
	s_waitcnt lgkmcnt(0)
	v_mul_f32_e32 v168, v88, v78
	v_mul_f32_e32 v169, v88, v82
	v_pk_mul_f32 v[164:165], v[168:169], s[20:21] op_sel_hi:[1,0]
	v_pk_fma_f32 v[172:173], v[168:169], s[22:23], v[96:97] op_sel_hi:[1,0,0]
	v_pk_fma_f32 v[162:163], v[164:165], v[168:169], v[90:91] op_sel_hi:[1,1,0]
	v_pk_mul_f32 v[164:165], v[172:173], v[172:173] neg_lo:[0,1] neg_hi:[0,1]
	v_exp_f32_e32 v166, v168
	v_exp_f32_e32 v167, v169
	v_exp_f32_e64 v170, -v168
	v_exp_f32_e64 v171, -v169
	v_exp_f32_e32 v162, v162
	v_exp_f32_e32 v164, v164
	v_exp_f32_e32 v165, v165
	v_exp_f32_e32 v163, v163
	v_pk_mul_f32 v[168:169], v[166:167], v[166:167]
	v_pk_mul_f32 v[172:173], v[170:171], v[170:171]
	v_pk_add_f32 v[94:95], v[94:95], v[164:165]
	v_pk_mul_f32 v[164:165], v[166:167], v[162:163]
	v_pk_fma_f32 v[106:107], v[166:167], v[162:163], v[106:107]
	v_pk_mul_f32 v[166:167], v[170:171], v[162:163]
	v_pk_fma_f32 v[108:109], v[170:171], v[162:163], v[108:109]
	v_pk_mul_f32 v[162:163], v[168:169], v[164:165]
	v_pk_fma_f32 v[104:105], v[168:169], v[164:165], v[104:105]
	v_pk_mul_f32 v[164:165], v[172:173], v[166:167]
	v_pk_fma_f32 v[110:111], v[172:173], v[166:167], v[110:111]
	v_pk_mul_f32 v[166:167], v[168:169], v[162:163]
	v_pk_fma_f32 v[102:103], v[168:169], v[162:163], v[102:103]
	v_pk_mul_f32 v[162:163], v[172:173], v[164:165]
	v_pk_fma_f32 v[112:113], v[172:173], v[164:165], v[112:113]
	v_pk_mul_f32 v[164:165], v[168:169], v[166:167]
	v_pk_fma_f32 v[100:101], v[168:169], v[166:167], v[100:101]
	v_pk_mul_f32 v[166:167], v[172:173], v[162:163]
	v_pk_fma_f32 v[114:115], v[172:173], v[162:163], v[114:115]
	v_pk_fma_f32 v[98:99], v[168:169], v[164:165], v[98:99]
	v_pk_fma_f32 v[116:117], v[172:173], v[166:167], v[116:117]
	v_mul_f32_e32 v168, v89, v79
	v_mul_f32_e32 v169, v89, v83
	v_pk_mul_f32 v[164:165], v[168:169], s[20:21] op_sel_hi:[1,0]
	v_pk_fma_f32 v[172:173], v[168:169], s[22:23], v[96:97] op_sel_hi:[1,0,0]
	v_pk_fma_f32 v[162:163], v[164:165], v[168:169], v[90:91] op_sel:[0,0,1] op_sel_hi:[1,1,1]
	v_pk_mul_f32 v[164:165], v[172:173], v[172:173] neg_lo:[0,1] neg_hi:[0,1]
	v_exp_f32_e32 v166, v168
	v_exp_f32_e32 v167, v169
	v_exp_f32_e64 v170, -v168
	v_exp_f32_e64 v171, -v169
	v_exp_f32_e32 v162, v162
	v_exp_f32_e32 v164, v164
	v_exp_f32_e32 v165, v165
	v_exp_f32_e32 v163, v163
	v_pk_mul_f32 v[168:169], v[166:167], v[166:167]
	v_pk_mul_f32 v[172:173], v[170:171], v[170:171]
	v_pk_add_f32 v[94:95], v[94:95], v[164:165]
	v_pk_mul_f32 v[164:165], v[166:167], v[162:163]
	v_pk_fma_f32 v[106:107], v[166:167], v[162:163], v[106:107]
	v_pk_mul_f32 v[166:167], v[170:171], v[162:163]
	v_pk_fma_f32 v[108:109], v[170:171], v[162:163], v[108:109]
	v_pk_mul_f32 v[162:163], v[168:169], v[164:165]
	v_pk_fma_f32 v[104:105], v[168:169], v[164:165], v[104:105]
	v_pk_mul_f32 v[164:165], v[172:173], v[166:167]
	v_pk_fma_f32 v[110:111], v[172:173], v[166:167], v[110:111]
	v_pk_mul_f32 v[166:167], v[168:169], v[162:163]
	v_pk_fma_f32 v[102:103], v[168:169], v[162:163], v[102:103]
	v_pk_mul_f32 v[162:163], v[172:173], v[164:165]
	v_pk_fma_f32 v[112:113], v[172:173], v[164:165], v[112:113]
	v_pk_mul_f32 v[164:165], v[168:169], v[166:167]
	v_pk_fma_f32 v[100:101], v[168:169], v[166:167], v[100:101]
	v_pk_mul_f32 v[166:167], v[172:173], v[162:163]
	v_pk_fma_f32 v[114:115], v[172:173], v[162:163], v[114:115]
	v_pk_fma_f32 v[98:99], v[168:169], v[164:165], v[98:99]
	v_pk_fma_f32 v[116:117], v[172:173], v[166:167], v[116:117]
	s_cmp_eq_u32 s3, 0
	s_cbranch_scc1 .Lret0
	s_cmp_eq_u32 s3, 1
	s_cbranch_scc1 .Lret1
	s_cmp_eq_u32 s3, 2
	s_cbranch_scc1 .Lret2
